# grid barrier: every waiter (non-leaders and XCD leaders) polls the cross-XCD arrival counter TOP against its round target instead of waiting for the TOPGEN/XGEN release relays
# speedup vs baseline: 1.0156x; 1.0002x over previous
.LBB0_66:
	s_or_b64 exec, exec, s[6:7]
	v_cvt_f32_u32_e32 v5, v3
	s_waitcnt vmcnt(0)
	v_readfirstlane_b32 s4, v4
	v_sub_u32_e32 v4, 0, v3
	v_rcp_iflag_f32_e32 v5, v5
	v_add_u32_e32 v6, s4, v2
	v_mul_f32_e32 v5, 0x4f7ffffe, v5
	v_cvt_u32_f32_e32 v5, v5
	v_mul_lo_u32 v2, v4, v5
	v_mul_hi_u32 v2, v5, v2
	v_add_u32_e32 v2, v5, v2
	v_mul_hi_u32 v2, v6, v2
	v_mul_lo_u32 v4, v2, v3
	v_sub_u32_e32 v4, v6, v4
	v_add_u32_e32 v5, 1, v2
	v_cmp_ge_u32_e32 vcc, v4, v3
	s_nop 1
	v_cndmask_b32_e32 v2, v2, v5, vcc
	v_sub_u32_e32 v5, v4, v3
	v_cndmask_b32_e32 v4, v4, v5, vcc
	v_add_u32_e32 v5, 1, v2
	v_cmp_ge_u32_e32 vcc, v4, v3
	v_add_u32_e32 v4, 1, v6
	s_nop 0
	v_cndmask_b32_e32 v2, v2, v5, vcc
	v_mul_lo_u32 v5, v3, v2
	v_add_u32_e32 v3, v5, v3
	v_cmp_ne_u32_e32 vcc, v4, v3
	s_and_saveexec_b64 s[4:5], vcc
	s_xor_b64 s[4:5], exec, s[4:5]
	s_cbranch_execz .LBB0_80
	s_waitcnt lgkmcnt(0)
	v_readlane_b32 s10, v255, 4
	v_readlane_b32 s11, v255, 5
	s_add_u32 s10, s10, 0x3400
	s_addc_u32 s11, s11, 0
	v_mov_b32_e32 v1, 0x20164
	ds_read_b32 v1, v1
	v_add_u32_e32 v2, 1, v2
	s_waitcnt lgkmcnt(0)
	v_mul_lo_u32 v2, v2, v1
	v_mov_b32_e32 v1, 0
	global_load_dword v1, v1, s[10:11] sc1
	s_waitcnt vmcnt(0)
	v_cmp_gt_u32_e32 vcc, v2, v1
	s_and_saveexec_b64 s[6:7], vcc
	s_cbranch_execz .LBB0_79
	v_readlane_b32 s8, v255, 2
	v_readlane_b32 s9, v255, 3
	s_add_u32 s8, s8, 0x4200
	s_addc_u32 s9, s9, 0
	s_mov_b32 s22, 1
	s_mov_b64 s[12:13], 0
	v_mov_b32_e32 v1, 0
	s_branch .LBB0_70

.LBB0_74:
	global_load_dword v3, v1, s[10:11] sc1
	s_add_i32 s22, s22, 1
	s_mov_b64 s[18:19], -1
	s_waitcnt vmcnt(0)
	v_cmp_le_u32_e32 vcc, v2, v3
	s_orn2_b64 s[16:17], vcc, exec
	s_branch .LBB0_69

.LBB0_83:
	s_or_b64 exec, exec, s[6:7]
	v_cvt_f32_u32_e32 v4, v1
	s_waitcnt vmcnt(0)
	v_readfirstlane_b32 s4, v3
	s_mov_b64 s[8:9], -1
	v_rcp_iflag_f32_e32 v4, v4
	v_add_u32_e32 v2, s4, v2
	v_add_u32_e32 v5, 1, v2
	v_readlane_b32 s4, v255, 2
	v_mul_f32_e32 v3, 0x4f7ffffe, v4
	v_cvt_u32_f32_e32 v3, v3
	v_sub_u32_e32 v4, 0, v1
	v_readlane_b32 s5, v255, 3
	s_add_u32 s6, s4, 0x7500
	v_mul_lo_u32 v4, v4, v3
	v_mul_hi_u32 v4, v3, v4
	v_add_u32_e32 v3, v3, v4
	v_mul_hi_u32 v3, v2, v3
	v_mul_lo_u32 v4, v3, v1
	v_sub_u32_e32 v2, v2, v4
	v_add_u32_e32 v6, 1, v3
	v_cmp_ge_u32_e32 vcc, v2, v1
	v_sub_u32_e32 v4, v2, v1
	s_addc_u32 s7, s5, 0
	v_cndmask_b32_e32 v3, v3, v6, vcc
	v_cndmask_b32_e32 v2, v2, v4, vcc
	v_add_u32_e32 v4, 1, v3
	v_cmp_ge_u32_e32 vcc, v2, v1
	s_nop 1
	v_cndmask_b32_e32 v4, v3, v4, vcc
	v_mul_lo_u32 v2, v1, v4
	v_add_u32_e32 v1, v2, v1
	v_mov_b32_e32 v4, v1
	v_cmp_ne_u32_e32 vcc, v5, v1
	v_mov_b64_e32 v[2:3], s[6:7]
	s_and_saveexec_b64 s[4:5], vcc
	s_cbranch_execz .LBB0_95
	v_mov_b32_e32 v1, 0
	global_load_dword v2, v1, s[6:7] offset:-256 sc1
	s_mov_b64 s[12:13], 0
	s_waitcnt vmcnt(0)
	v_cmp_gt_u32_e32 vcc, v4, v2
	s_and_saveexec_b64 s[10:11], vcc
	s_cbranch_execz .LBB0_94
	v_readlane_b32 s8, v255, 2
	v_readlane_b32 s9, v255, 3
	s_add_u32 s8, s8, 0x4200
	s_addc_u32 s9, s9, 0
	s_mov_b32 s22, 1
	s_branch .LBB0_87

.LBB0_91:
	global_load_dword v2, v1, s[6:7] offset:-256 sc1
	s_add_i32 s22, s22, 1
	s_mov_b64 s[16:17], -1
	s_waitcnt vmcnt(0)
	v_cmp_le_u32_e32 vcc, v4, v2
	s_orn2_b64 s[20:21], vcc, exec
	s_branch .LBB0_86

.LBB0_403:
	s_or_b64 exec, exec, s[6:7]
	v_cvt_f32_u32_e32 v6, v4
	s_waitcnt vmcnt(0)
	v_readfirstlane_b32 s4, v5
	v_sub_u32_e32 v5, 0, v4
	v_rcp_iflag_f32_e32 v6, v6
	v_add_u32_e32 v7, s4, v3
	v_mul_f32_e32 v6, 0x4f7ffffe, v6
	v_cvt_u32_f32_e32 v6, v6
	v_mul_lo_u32 v3, v5, v6
	v_mul_hi_u32 v3, v6, v3
	v_add_u32_e32 v3, v6, v3
	v_mul_hi_u32 v3, v7, v3
	v_mul_lo_u32 v5, v3, v4
	v_sub_u32_e32 v5, v7, v5
	v_add_u32_e32 v6, 1, v3
	v_cmp_ge_u32_e32 vcc, v5, v4
	s_nop 1
	v_cndmask_b32_e32 v3, v3, v6, vcc
	v_sub_u32_e32 v6, v5, v4
	v_cndmask_b32_e32 v5, v5, v6, vcc
	v_add_u32_e32 v6, 1, v3
	v_cmp_ge_u32_e32 vcc, v5, v4
	v_add_u32_e32 v5, 1, v7
	s_nop 0
	v_cndmask_b32_e32 v3, v3, v6, vcc
	v_mul_lo_u32 v6, v4, v3
	v_add_u32_e32 v4, v6, v4
	v_cmp_ne_u32_e32 vcc, v5, v4
	s_and_saveexec_b64 s[4:5], vcc
	s_xor_b64 s[4:5], exec, s[4:5]
	s_cbranch_execz .LBB0_417
	s_waitcnt lgkmcnt(0)
	v_readlane_b32 s10, v255, 4
	v_readlane_b32 s11, v255, 5
	s_add_u32 s10, s10, 0x3400
	s_addc_u32 s11, s11, 0
	v_mov_b32_e32 v2, 0x20164
	ds_read_b32 v2, v2
	v_add_u32_e32 v3, 1, v3
	s_waitcnt lgkmcnt(0)
	v_mul_lo_u32 v3, v3, v2
	v_mov_b32_e32 v2, 0
	global_load_dword v2, v2, s[10:11] sc1
	s_waitcnt vmcnt(0)
	v_cmp_gt_u32_e32 vcc, v3, v2
	s_and_saveexec_b64 s[6:7], vcc
	s_cbranch_execz .LBB0_416
	v_readlane_b32 s8, v255, 2
	v_readlane_b32 s9, v255, 3
	s_add_u32 s8, s8, 0x4200
	s_addc_u32 s9, s9, 0
	s_mov_b32 s22, 1
	s_mov_b64 s[12:13], 0
	v_mov_b32_e32 v2, 0
	s_branch .LBB0_407

.LBB0_411:
	global_load_dword v4, v2, s[10:11] sc1
	s_add_i32 s22, s22, 1
	s_mov_b64 s[18:19], -1
	s_waitcnt vmcnt(0)
	v_cmp_le_u32_e32 vcc, v3, v4
	s_orn2_b64 s[16:17], vcc, exec
	s_branch .LBB0_406

.LBB0_420:
	s_or_b64 exec, exec, s[6:7]
	v_cvt_f32_u32_e32 v5, v2
	s_waitcnt vmcnt(0)
	v_readfirstlane_b32 s4, v4
	s_mov_b64 s[8:9], -1
	v_rcp_iflag_f32_e32 v5, v5
	v_add_u32_e32 v3, s4, v3
	v_add_u32_e32 v6, 1, v3
	v_readlane_b32 s4, v255, 2
	v_mul_f32_e32 v4, 0x4f7ffffe, v5
	v_cvt_u32_f32_e32 v4, v4
	v_sub_u32_e32 v5, 0, v2
	v_readlane_b32 s5, v255, 3
	s_add_u32 s6, s4, 0x7500
	v_mul_lo_u32 v5, v5, v4
	v_mul_hi_u32 v5, v4, v5
	v_add_u32_e32 v4, v4, v5
	v_mul_hi_u32 v4, v3, v4
	v_mul_lo_u32 v5, v4, v2
	v_sub_u32_e32 v3, v3, v5
	v_add_u32_e32 v7, 1, v4
	v_cmp_ge_u32_e32 vcc, v3, v2
	v_sub_u32_e32 v5, v3, v2
	s_addc_u32 s7, s5, 0
	v_cndmask_b32_e32 v4, v4, v7, vcc
	v_cndmask_b32_e32 v3, v3, v5, vcc
	v_add_u32_e32 v5, 1, v4
	v_cmp_ge_u32_e32 vcc, v3, v2
	s_nop 1
	v_cndmask_b32_e32 v4, v4, v5, vcc
	v_mul_lo_u32 v3, v2, v4
	v_add_u32_e32 v2, v3, v2
	v_mov_b32_e32 v4, v2
	v_cmp_ne_u32_e32 vcc, v6, v2
	v_mov_b64_e32 v[2:3], s[6:7]
	s_and_saveexec_b64 s[4:5], vcc
	s_cbranch_execz .LBB0_432
	v_mov_b32_e32 v2, 0
	global_load_dword v3, v2, s[6:7] offset:-256 sc1
	s_mov_b64 s[12:13], 0
	s_waitcnt vmcnt(0)
	v_cmp_gt_u32_e32 vcc, v4, v3
	s_and_saveexec_b64 s[10:11], vcc
	s_cbranch_execz .LBB0_431
	v_readlane_b32 s8, v255, 2
	v_readlane_b32 s9, v255, 3
	s_add_u32 s8, s8, 0x4200
	s_addc_u32 s9, s9, 0
	s_mov_b32 s22, 1
	s_branch .LBB0_424

.LBB0_428:
	global_load_dword v3, v2, s[6:7] offset:-256 sc1
	s_add_i32 s22, s22, 1
	s_mov_b64 s[16:17], -1
	s_waitcnt vmcnt(0)
	v_cmp_le_u32_e32 vcc, v4, v3
	s_orn2_b64 s[20:21], vcc, exec
	s_branch .LBB0_423

.LBB0_495:
	s_or_b64 exec, exec, s[6:7]
	v_cvt_f32_u32_e32 v6, v4
	s_waitcnt vmcnt(0)
	v_readfirstlane_b32 s4, v5
	v_sub_u32_e32 v5, 0, v4
	v_rcp_iflag_f32_e32 v6, v6
	v_add_u32_e32 v7, s4, v3
	v_mul_f32_e32 v6, 0x4f7ffffe, v6
	v_cvt_u32_f32_e32 v6, v6
	v_mul_lo_u32 v3, v5, v6
	v_mul_hi_u32 v3, v6, v3
	v_add_u32_e32 v3, v6, v3
	v_mul_hi_u32 v3, v7, v3
	v_mul_lo_u32 v5, v3, v4
	v_sub_u32_e32 v5, v7, v5
	v_add_u32_e32 v6, 1, v3
	v_cmp_ge_u32_e32 vcc, v5, v4
	s_nop 1
	v_cndmask_b32_e32 v3, v3, v6, vcc
	v_sub_u32_e32 v6, v5, v4
	v_cndmask_b32_e32 v5, v5, v6, vcc
	v_add_u32_e32 v6, 1, v3
	v_cmp_ge_u32_e32 vcc, v5, v4
	v_add_u32_e32 v5, 1, v7
	s_nop 0
	v_cndmask_b32_e32 v3, v3, v6, vcc
	v_mul_lo_u32 v6, v4, v3
	v_add_u32_e32 v4, v6, v4
	v_cmp_ne_u32_e32 vcc, v5, v4
	s_and_saveexec_b64 s[4:5], vcc
	s_xor_b64 s[4:5], exec, s[4:5]
	s_cbranch_execz .LBB0_509
	s_waitcnt lgkmcnt(0)
	v_readlane_b32 s12, v255, 4
	v_readlane_b32 s13, v255, 5
	s_add_u32 s12, s12, 0x3400
	s_addc_u32 s13, s13, 0
	v_mov_b32_e32 v2, 0x20164
	ds_read_b32 v2, v2
	v_add_u32_e32 v3, 1, v3
	s_waitcnt lgkmcnt(0)
	v_mul_lo_u32 v3, v3, v2
	v_mov_b32_e32 v2, 0
	global_load_dword v2, v2, s[12:13] sc1
	s_waitcnt vmcnt(0)
	v_cmp_gt_u32_e32 vcc, v3, v2
	s_and_saveexec_b64 s[6:7], vcc
	s_cbranch_execz .LBB0_508
	v_readlane_b32 s10, v255, 2
	v_readlane_b32 s11, v255, 3
	s_add_u32 s10, s10, 0x4200
	s_addc_u32 s11, s11, 0
	s_mov_b32 s24, 1
	s_mov_b64 s[14:15], 0
	v_mov_b32_e32 v2, 0
	s_branch .LBB0_499

.LBB0_503:
	global_load_dword v4, v2, s[12:13] sc1
	s_add_i32 s24, s24, 1
	s_mov_b64 s[20:21], -1
	s_waitcnt vmcnt(0)
	v_cmp_le_u32_e32 vcc, v3, v4
	s_orn2_b64 s[18:19], vcc, exec
	s_branch .LBB0_498

.LBB0_512:
	s_or_b64 exec, exec, s[6:7]
	v_cvt_f32_u32_e32 v5, v2
	s_waitcnt vmcnt(0)
	v_readfirstlane_b32 s4, v4
	s_mov_b64 s[10:11], -1
	v_rcp_iflag_f32_e32 v5, v5
	v_add_u32_e32 v3, s4, v3
	v_add_u32_e32 v6, 1, v3
	v_readlane_b32 s4, v255, 2
	v_mul_f32_e32 v4, 0x4f7ffffe, v5
	v_cvt_u32_f32_e32 v4, v4
	v_sub_u32_e32 v5, 0, v2
	v_readlane_b32 s5, v255, 3
	s_add_u32 s6, s4, 0x7500
	v_mul_lo_u32 v5, v5, v4
	v_mul_hi_u32 v5, v4, v5
	v_add_u32_e32 v4, v4, v5
	v_mul_hi_u32 v4, v3, v4
	v_mul_lo_u32 v5, v4, v2
	v_sub_u32_e32 v3, v3, v5
	v_add_u32_e32 v7, 1, v4
	v_cmp_ge_u32_e32 vcc, v3, v2
	v_sub_u32_e32 v5, v3, v2
	s_addc_u32 s7, s5, 0
	v_cndmask_b32_e32 v4, v4, v7, vcc
	v_cndmask_b32_e32 v3, v3, v5, vcc
	v_add_u32_e32 v5, 1, v4
	v_cmp_ge_u32_e32 vcc, v3, v2
	s_nop 1
	v_cndmask_b32_e32 v4, v4, v5, vcc
	v_mul_lo_u32 v3, v2, v4
	v_add_u32_e32 v2, v3, v2
	v_mov_b32_e32 v4, v2
	v_cmp_ne_u32_e32 vcc, v6, v2
	v_mov_b64_e32 v[2:3], s[6:7]
	s_and_saveexec_b64 s[4:5], vcc
	s_cbranch_execz .LBB0_524
	v_mov_b32_e32 v2, 0
	global_load_dword v3, v2, s[6:7] offset:-256 sc1
	s_mov_b64 s[14:15], 0
	s_waitcnt vmcnt(0)
	v_cmp_gt_u32_e32 vcc, v4, v3
	s_and_saveexec_b64 s[12:13], vcc
	s_cbranch_execz .LBB0_523
	v_readlane_b32 s10, v255, 2
	v_readlane_b32 s11, v255, 3
	s_add_u32 s10, s10, 0x4200
	s_addc_u32 s11, s11, 0
	s_mov_b32 s24, 1
	s_branch .LBB0_516

.LBB0_520:
	global_load_dword v3, v2, s[6:7] offset:-256 sc1
	s_add_i32 s24, s24, 1
	s_mov_b64 s[18:19], -1
	s_waitcnt vmcnt(0)
	v_cmp_le_u32_e32 vcc, v4, v3
	s_orn2_b64 s[22:23], vcc, exec
	s_branch .LBB0_515

.LBB0_673:
	s_or_b64 exec, exec, s[6:7]
	v_cvt_f32_u32_e32 v5, v3
	s_waitcnt vmcnt(0)
	v_readfirstlane_b32 s4, v4
	v_sub_u32_e32 v4, 0, v3
	v_rcp_iflag_f32_e32 v5, v5
	v_add_u32_e32 v6, s4, v2
	v_mul_f32_e32 v5, 0x4f7ffffe, v5
	v_cvt_u32_f32_e32 v5, v5
	v_mul_lo_u32 v2, v4, v5
	v_mul_hi_u32 v2, v5, v2
	v_add_u32_e32 v2, v5, v2
	v_mul_hi_u32 v2, v6, v2
	v_mul_lo_u32 v4, v2, v3
	v_sub_u32_e32 v4, v6, v4
	v_add_u32_e32 v5, 1, v2
	v_cmp_ge_u32_e32 vcc, v4, v3
	s_nop 1
	v_cndmask_b32_e32 v2, v2, v5, vcc
	v_sub_u32_e32 v5, v4, v3
	v_cndmask_b32_e32 v4, v4, v5, vcc
	v_add_u32_e32 v5, 1, v2
	v_cmp_ge_u32_e32 vcc, v4, v3
	v_add_u32_e32 v4, 1, v6
	s_nop 0
	v_cndmask_b32_e32 v2, v2, v5, vcc
	v_mul_lo_u32 v5, v3, v2
	v_add_u32_e32 v3, v5, v3
	v_cmp_ne_u32_e32 vcc, v4, v3
	s_and_saveexec_b64 s[4:5], vcc
	s_xor_b64 s[4:5], exec, s[4:5]
	s_cbranch_execz .LBB0_687
	s_waitcnt lgkmcnt(0)
	v_readlane_b32 s12, v255, 4
	v_readlane_b32 s13, v255, 5
	s_add_u32 s12, s12, 0x3400
	s_addc_u32 s13, s13, 0
	v_mov_b32_e32 v1, 0x20164
	ds_read_b32 v1, v1
	v_add_u32_e32 v2, 1, v2
	s_waitcnt lgkmcnt(0)
	v_mul_lo_u32 v2, v2, v1
	v_mov_b32_e32 v1, 0
	global_load_dword v1, v1, s[12:13] sc1
	s_waitcnt vmcnt(0)
	v_cmp_gt_u32_e32 vcc, v2, v1
	s_and_saveexec_b64 s[6:7], vcc
	s_cbranch_execz .LBB0_686
	v_readlane_b32 s10, v255, 2
	v_readlane_b32 s11, v255, 3
	s_add_u32 s10, s10, 0x4200
	s_addc_u32 s11, s11, 0
	s_mov_b32 s24, 1
	s_mov_b64 s[14:15], 0
	v_mov_b32_e32 v1, 0
	s_branch .LBB0_677

.LBB0_681:
	global_load_dword v3, v1, s[12:13] sc1
	s_add_i32 s24, s24, 1
	s_mov_b64 s[20:21], -1
	s_waitcnt vmcnt(0)
	v_cmp_le_u32_e32 vcc, v2, v3
	s_orn2_b64 s[18:19], vcc, exec
	s_branch .LBB0_676

.LBB0_690:
	s_or_b64 exec, exec, s[6:7]
	v_cvt_f32_u32_e32 v4, v1
	s_waitcnt vmcnt(0)
	v_readfirstlane_b32 s4, v3
	s_mov_b64 s[10:11], -1
	v_rcp_iflag_f32_e32 v4, v4
	v_add_u32_e32 v2, s4, v2
	v_add_u32_e32 v5, 1, v2
	v_readlane_b32 s4, v255, 2
	v_mul_f32_e32 v3, 0x4f7ffffe, v4
	v_cvt_u32_f32_e32 v3, v3
	v_sub_u32_e32 v4, 0, v1
	v_readlane_b32 s5, v255, 3
	s_add_u32 s6, s4, 0x7500
	v_mul_lo_u32 v4, v4, v3
	v_mul_hi_u32 v4, v3, v4
	v_add_u32_e32 v3, v3, v4
	v_mul_hi_u32 v3, v2, v3
	v_mul_lo_u32 v4, v3, v1
	v_sub_u32_e32 v2, v2, v4
	v_add_u32_e32 v6, 1, v3
	v_cmp_ge_u32_e32 vcc, v2, v1
	v_sub_u32_e32 v4, v2, v1
	s_addc_u32 s7, s5, 0
	v_cndmask_b32_e32 v3, v3, v6, vcc
	v_cndmask_b32_e32 v2, v2, v4, vcc
	v_add_u32_e32 v4, 1, v3
	v_cmp_ge_u32_e32 vcc, v2, v1
	s_nop 1
	v_cndmask_b32_e32 v4, v3, v4, vcc
	v_mul_lo_u32 v2, v1, v4
	v_add_u32_e32 v1, v2, v1
	v_mov_b32_e32 v4, v1
	v_cmp_ne_u32_e32 vcc, v5, v1
	v_mov_b64_e32 v[2:3], s[6:7]
	s_and_saveexec_b64 s[4:5], vcc
	s_cbranch_execz .LBB0_702
	v_mov_b32_e32 v1, 0
	global_load_dword v2, v1, s[6:7] offset:-256 sc1
	s_mov_b64 s[14:15], 0
	s_waitcnt vmcnt(0)
	v_cmp_gt_u32_e32 vcc, v4, v2
	s_and_saveexec_b64 s[12:13], vcc
	s_cbranch_execz .LBB0_701
	v_readlane_b32 s10, v255, 2
	v_readlane_b32 s11, v255, 3
	s_add_u32 s10, s10, 0x4200
	s_addc_u32 s11, s11, 0
	s_mov_b32 s24, 1
	s_branch .LBB0_694

.LBB0_698:
	global_load_dword v2, v1, s[6:7] offset:-256 sc1
	s_add_i32 s24, s24, 1
	s_mov_b64 s[18:19], -1
	s_waitcnt vmcnt(0)
	v_cmp_le_u32_e32 vcc, v4, v2
	s_orn2_b64 s[22:23], vcc, exec
	s_branch .LBB0_693

.LBB0_749:
	s_or_b64 exec, exec, s[6:7]
	v_cvt_f32_u32_e32 v4, v2
	s_waitcnt vmcnt(0)
	v_readfirstlane_b32 s4, v3
	v_sub_u32_e32 v3, 0, v2
	v_rcp_iflag_f32_e32 v4, v4
	v_add_u32_e32 v5, s4, v1
	v_mul_f32_e32 v4, 0x4f7ffffe, v4
	v_cvt_u32_f32_e32 v4, v4
	v_mul_lo_u32 v1, v3, v4
	v_mul_hi_u32 v1, v4, v1
	v_add_u32_e32 v1, v4, v1
	v_mul_hi_u32 v1, v5, v1
	v_mul_lo_u32 v3, v1, v2
	v_sub_u32_e32 v3, v5, v3
	v_add_u32_e32 v4, 1, v1
	v_cmp_ge_u32_e32 vcc, v3, v2
	s_nop 1
	v_cndmask_b32_e32 v1, v1, v4, vcc
	v_sub_u32_e32 v4, v3, v2
	v_cndmask_b32_e32 v3, v3, v4, vcc
	v_add_u32_e32 v4, 1, v1
	v_cmp_ge_u32_e32 vcc, v3, v2
	v_add_u32_e32 v3, 1, v5
	s_nop 0
	v_cndmask_b32_e32 v1, v1, v4, vcc
	v_mul_lo_u32 v4, v2, v1
	v_add_u32_e32 v2, v4, v2
	v_cmp_ne_u32_e32 vcc, v3, v2
	s_and_saveexec_b64 s[4:5], vcc
	s_xor_b64 s[4:5], exec, s[4:5]
	s_cbranch_execz .LBB0_763
	s_waitcnt lgkmcnt(0)
	v_readlane_b32 s10, v255, 4
	v_readlane_b32 s11, v255, 5
	s_add_u32 s10, s10, 0x3400
	s_addc_u32 s11, s11, 0
	v_mov_b32_e32 v0, 0x20164
	ds_read_b32 v0, v0
	v_add_u32_e32 v1, 1, v1
	s_waitcnt lgkmcnt(0)
	v_mul_lo_u32 v1, v1, v0
	v_mov_b32_e32 v0, 0
	global_load_dword v0, v0, s[10:11] sc1
	s_waitcnt vmcnt(0)
	v_cmp_gt_u32_e32 vcc, v1, v0
	s_and_saveexec_b64 s[6:7], vcc
	s_cbranch_execz .LBB0_762
	v_readlane_b32 s8, v255, 2
	v_readlane_b32 s9, v255, 3
	s_add_u32 s8, s8, 0x4200
	s_addc_u32 s9, s9, 0
	s_mov_b32 s22, 1
	s_mov_b64 s[12:13], 0
	v_mov_b32_e32 v0, 0
	s_branch .LBB0_753

.LBB0_757:
	global_load_dword v2, v0, s[10:11] sc1
	s_add_i32 s22, s22, 1
	s_mov_b64 s[18:19], -1
	s_waitcnt vmcnt(0)
	v_cmp_le_u32_e32 vcc, v1, v2
	s_orn2_b64 s[16:17], vcc, exec
	s_branch .LBB0_752

.LBB0_766:
	s_or_b64 exec, exec, s[6:7]
	v_cvt_f32_u32_e32 v3, v0
	s_waitcnt vmcnt(0)
	v_readfirstlane_b32 s4, v2
	s_mov_b64 s[8:9], -1
	v_rcp_iflag_f32_e32 v3, v3
	v_add_u32_e32 v1, s4, v1
	v_add_u32_e32 v4, 1, v1
	v_readlane_b32 s4, v255, 2
	v_mul_f32_e32 v2, 0x4f7ffffe, v3
	v_cvt_u32_f32_e32 v2, v2
	v_sub_u32_e32 v3, 0, v0
	v_readlane_b32 s5, v255, 3
	s_add_u32 s6, s4, 0x7500
	v_mul_lo_u32 v3, v3, v2
	v_mul_hi_u32 v3, v2, v3
	v_add_u32_e32 v2, v2, v3
	v_mul_hi_u32 v2, v1, v2
	v_mul_lo_u32 v3, v2, v0
	v_sub_u32_e32 v1, v1, v3
	v_add_u32_e32 v5, 1, v2
	v_cmp_ge_u32_e32 vcc, v1, v0
	v_sub_u32_e32 v3, v1, v0
	s_addc_u32 s7, s5, 0
	v_cndmask_b32_e32 v2, v2, v5, vcc
	v_cndmask_b32_e32 v1, v1, v3, vcc
	v_add_u32_e32 v3, 1, v2
	v_cmp_ge_u32_e32 vcc, v1, v0
	s_nop 1
	v_cndmask_b32_e32 v2, v2, v3, vcc
	v_mul_lo_u32 v1, v0, v2
	v_add_u32_e32 v0, v1, v0
	v_mov_b32_e32 v2, v0
	v_cmp_ne_u32_e32 vcc, v4, v0
	v_mov_b64_e32 v[0:1], s[6:7]
	s_and_saveexec_b64 s[4:5], vcc
	s_cbranch_execz .LBB0_778
	v_mov_b32_e32 v0, 0
	global_load_dword v1, v0, s[6:7] offset:-256 sc1
	s_mov_b64 s[12:13], 0
	s_waitcnt vmcnt(0)
	v_cmp_gt_u32_e32 vcc, v2, v1
	s_and_saveexec_b64 s[10:11], vcc
	s_cbranch_execz .LBB0_777
	v_readlane_b32 s8, v255, 2
	v_readlane_b32 s9, v255, 3
	s_add_u32 s8, s8, 0x4200
	s_addc_u32 s9, s9, 0
	s_mov_b32 s22, 1
	s_branch .LBB0_770

.LBB0_774:
	global_load_dword v1, v0, s[6:7] offset:-256 sc1
	s_add_i32 s22, s22, 1
	s_mov_b64 s[16:17], -1
	s_waitcnt vmcnt(0)
	v_cmp_le_u32_e32 vcc, v2, v1
	s_orn2_b64 s[20:21], vcc, exec
	s_branch .LBB0_769

.LBB0_835:
	s_or_b64 exec, exec, s[8:9]
	v_cvt_f32_u32_e32 v4, v2
	s_waitcnt vmcnt(0)
	v_readfirstlane_b32 s3, v3
	v_sub_u32_e32 v3, 0, v2
	v_rcp_iflag_f32_e32 v4, v4
	v_add_u32_e32 v5, s3, v1
	v_mul_f32_e32 v4, 0x4f7ffffe, v4
	v_cvt_u32_f32_e32 v4, v4
	v_mul_lo_u32 v1, v3, v4
	v_mul_hi_u32 v1, v4, v1
	v_add_u32_e32 v1, v4, v1
	v_mul_hi_u32 v1, v5, v1
	v_mul_lo_u32 v3, v1, v2
	v_sub_u32_e32 v3, v5, v3
	v_add_u32_e32 v4, 1, v1
	v_cmp_ge_u32_e32 vcc, v3, v2
	s_nop 1
	v_cndmask_b32_e32 v1, v1, v4, vcc
	v_sub_u32_e32 v4, v3, v2
	v_cndmask_b32_e32 v3, v3, v4, vcc
	v_add_u32_e32 v4, 1, v1
	v_cmp_ge_u32_e32 vcc, v3, v2
	v_add_u32_e32 v3, 1, v5
	s_nop 0
	v_cndmask_b32_e32 v1, v1, v4, vcc
	v_mul_lo_u32 v4, v2, v1
	v_add_u32_e32 v2, v4, v2
	v_cmp_ne_u32_e32 vcc, v3, v2
	s_and_saveexec_b64 s[6:7], vcc
	s_xor_b64 s[6:7], exec, s[6:7]
	s_cbranch_execz .LBB0_849
	s_waitcnt lgkmcnt(0)
	v_readlane_b32 s12, v255, 4
	v_readlane_b32 s13, v255, 5
	s_add_u32 s12, s12, 0x3400
	s_addc_u32 s13, s13, 0
	v_mov_b32_e32 v0, 0x20164
	ds_read_b32 v0, v0
	v_add_u32_e32 v1, 1, v1
	s_waitcnt lgkmcnt(0)
	v_mul_lo_u32 v1, v1, v0
	v_mov_b32_e32 v0, 0
	global_load_dword v0, v0, s[12:13] sc1
	s_waitcnt vmcnt(0)
	v_cmp_gt_u32_e32 vcc, v1, v0
	s_and_saveexec_b64 s[8:9], vcc
	s_cbranch_execz .LBB0_848
	v_readlane_b32 s10, v255, 2
	v_readlane_b32 s11, v255, 3
	s_add_u32 s10, s10, 0x4200
	s_addc_u32 s11, s11, 0
	s_mov_b32 s3, 1
	s_mov_b64 s[14:15], 0
	v_mov_b32_e32 v0, 0
	s_branch .LBB0_839

.LBB0_843:
	global_load_dword v2, v0, s[12:13] sc1
	s_add_i32 s3, s3, 1
	s_mov_b64 s[20:21], -1
	s_waitcnt vmcnt(0)
	v_cmp_le_u32_e32 vcc, v1, v2
	s_orn2_b64 s[18:19], vcc, exec
	s_branch .LBB0_838

.LBB0_852:
	s_or_b64 exec, exec, s[8:9]
	v_cvt_f32_u32_e32 v3, v0
	s_waitcnt vmcnt(0)
	v_readfirstlane_b32 s3, v2
	v_readlane_b32 s6, v255, 2
	v_readlane_b32 s7, v255, 3
	v_rcp_iflag_f32_e32 v3, v3
	v_add_u32_e32 v1, s3, v1
	v_add_u32_e32 v4, 1, v1
	s_add_u32 s8, s6, 0x7500
	v_mul_f32_e32 v2, 0x4f7ffffe, v3
	v_cvt_u32_f32_e32 v2, v2
	v_sub_u32_e32 v3, 0, v0
	s_addc_u32 s9, s7, 0
	s_mov_b64 s[10:11], -1
	v_mul_lo_u32 v3, v3, v2
	v_mul_hi_u32 v3, v2, v3
	v_add_u32_e32 v2, v2, v3
	v_mul_hi_u32 v2, v1, v2
	v_mul_lo_u32 v3, v2, v0
	v_sub_u32_e32 v1, v1, v3
	v_add_u32_e32 v5, 1, v2
	v_cmp_ge_u32_e32 vcc, v1, v0
	v_sub_u32_e32 v3, v1, v0
	s_nop 0
	v_cndmask_b32_e32 v2, v2, v5, vcc
	v_cndmask_b32_e32 v1, v1, v3, vcc
	v_add_u32_e32 v3, 1, v2
	v_cmp_ge_u32_e32 vcc, v1, v0
	s_nop 1
	v_cndmask_b32_e32 v2, v2, v3, vcc
	v_mul_lo_u32 v1, v0, v2
	v_add_u32_e32 v0, v1, v0
	v_mov_b32_e32 v2, v0
	v_cmp_ne_u32_e32 vcc, v4, v0
	v_mov_b64_e32 v[0:1], s[8:9]
	s_and_saveexec_b64 s[6:7], vcc
	s_cbranch_execz .LBB0_864
	v_mov_b32_e32 v0, 0
	global_load_dword v1, v0, s[8:9] offset:-256 sc1
	s_mov_b64 s[14:15], 0
	s_waitcnt vmcnt(0)
	v_cmp_gt_u32_e32 vcc, v2, v1
	s_and_saveexec_b64 s[12:13], vcc
	s_cbranch_execz .LBB0_863
	v_readlane_b32 s10, v255, 2
	v_readlane_b32 s11, v255, 3
	s_add_u32 s10, s10, 0x4200
	s_addc_u32 s11, s11, 0
	s_mov_b32 s3, 1
	s_branch .LBB0_856

.LBB0_860:
	global_load_dword v1, v0, s[8:9] offset:-256 sc1
	s_add_i32 s3, s3, 1
	s_mov_b64 s[18:19], -1
	s_waitcnt vmcnt(0)
	v_cmp_le_u32_e32 vcc, v2, v1
	s_orn2_b64 s[22:23], vcc, exec
	s_branch .LBB0_855
